# static priority raise for waves 0-3 (other half) over the DSA attention loop; on top of v26
# baseline (speedup 1.0000x reference)
.LBB0_714:
	s_cmp_ge_u32 s96, 4
	s_cbranch_scc1 .Lprio_x_a
	s_setprio 1
